# post2 phase: a token row's proj and x pieces requested up front instead of one round trip per chunk (on top of v19)
# baseline (speedup 1.0000x reference)
.LBB0_1670:
	s_or_b64 exec, exec, s[10:11]
	v_ashrrev_i32_e32 v2, 6, v4
	v_add_u32_e32 v2, s84, v2
	s_movk_i32 s3, 0x2000
	v_cmp_gt_i32_e32 vcc, s3, v2
	s_waitcnt lgkmcnt(0)
	s_barrier
	s_and_saveexec_b64 s[10:11], vcc
	s_cbranch_execz .LBB0_1675
	v_and_b32_e32 v3, 63, v4
	v_mov_b32_e32 v13, 0
	v_lshlrev_b32_e32 v12, 4, v3
	v_lshlrev_b32_e32 v10, 3, v3
	v_mov_b32_e32 v11, v13
	v_lshl_add_u64 v[4:5], s[8:9], 0, v[12:13]
	v_lshl_add_u64 v[6:7], s[16:17], 0, v[10:11]
	s_mov_b64 s[8:9], 0x40c00000
	s_add_u32 s12, s12, 0x54c00000
	v_lshl_add_u64 v[6:7], v[6:7], 0, s[8:9]
	v_lshl_add_u64 v[8:9], s[20:21], 0, v[10:11]
	s_mov_b64 s[8:9], 0x34400000
	s_addc_u32 s13, s13, 0
	v_lshl_add_u64 v[8:9], v[8:9], 0, s[8:9]
	v_lshl_add_u64 v[10:11], s[22:23], 0, v[10:11]
	s_mov_b64 s[8:9], 0x1a300000
	v_lshlrev_b32_e32 v14, 2, v3
	v_mov_b32_e32 v15, v13
	s_add_u32 s14, s14, 0x54c10000
	v_lshl_add_u64 v[10:11], v[10:11], 0, s[8:9]
	v_add_u32_e32 v86, 0, v12
	v_lshl_add_u64 v[12:13], s[18:19], 0, v[14:15]
	s_mov_b64 s[8:9], 0x50c00000
	s_addc_u32 s15, s15, 0
	v_lshl_add_u64 v[12:13], v[12:13], 0, s[8:9]
	v_cmp_eq_u32_e64 s[8:9], 0, v3
	s_lshl_b32 s20, s46, 3
	s_mov_b64 s[16:17], 0
	s_mov_b32 s21, 0xffff0000
	s_movk_i32 s22, 0x7fff
	s_movk_i32 s23, 0x1000
	s_movk_i32 s24, 0x3000
	v_mov_b32_e32 v87, 0x358637bd
	s_mov_b32 s25, 0x800000
	s_mov_b32 s26, 0xda24260
	s_mov_b32 s27, 0x40c0c00
	s_movk_i32 s28, 0x1fff
	v_mov_b32_e32 v88, 1
	s_mov_b64 s[98:99], 0x1000
	s_branch .LBB0_1673

.LBB0_1673:
	v_ashrrev_i32_e32 v3, 31, v2
	v_lshlrev_b64 v[52:53], 13, v[2:3]
	v_lshl_add_u64 v[42:43], v[6:7], 0, v[52:53]
	v_lshlrev_b64 v[16:17], 14, v[2:3]
	s_waitcnt lgkmcnt(0)
	v_lshl_add_u64 v[66:67], v[4:5], 0, v[16:17]
	v_lshl_add_u64 v[242:243], v[42:43], 0, s[98:99]
	v_lshl_add_u64 v[244:245], v[66:67], 0, s[98:99]
	v_lshl_add_u64 v[246:247], v[244:245], 0, s[98:99]
	v_lshl_add_u64 v[248:249], v[246:247], 0, s[98:99]
	global_load_dwordx2 v[178:179], v[42:43], off
	global_load_dwordx2 v[180:181], v[42:43], off offset:512
	global_load_dwordx2 v[182:183], v[42:43], off offset:1024
	global_load_dwordx2 v[184:185], v[42:43], off offset:1536
	global_load_dwordx2 v[186:187], v[42:43], off offset:2048
	global_load_dwordx2 v[188:189], v[42:43], off offset:2560
	global_load_dwordx2 v[190:191], v[42:43], off offset:3072
	global_load_dwordx2 v[192:193], v[42:43], off offset:3584
	global_load_dwordx2 v[194:195], v[242:243], off
	global_load_dwordx2 v[196:197], v[242:243], off offset:512
	global_load_dwordx2 v[198:199], v[242:243], off offset:1024
	global_load_dwordx2 v[200:201], v[242:243], off offset:1536
	global_load_dwordx2 v[202:203], v[242:243], off offset:2048
	global_load_dwordx2 v[204:205], v[242:243], off offset:2560
	global_load_dwordx2 v[206:207], v[242:243], off offset:3072
	global_load_dwordx2 v[208:209], v[242:243], off offset:3584
	global_load_dwordx4 v[210:213], v[66:67], off
	global_load_dwordx4 v[214:217], v[66:67], off offset:1024
	global_load_dwordx4 v[218:221], v[66:67], off offset:2048
	global_load_dwordx4 v[222:225], v[66:67], off offset:3072
	global_load_dwordx4 v[226:229], v[244:245], off
	global_load_dwordx4 v[230:233], v[244:245], off offset:1024
	global_load_dwordx4 v[234:237], v[244:245], off offset:2048
	global_load_dwordx4 v[238:241], v[244:245], off offset:3072
	s_waitcnt vmcnt(7)
	v_mov_b32_e32 v14, v178
	v_mov_b32_e32 v15, v179
	v_mov_b32_e32 v16, v210
	v_mov_b32_e32 v17, v211
	v_mov_b32_e32 v18, v212
	v_mov_b32_e32 v19, v213
	v_lshl_add_u64 v[46:47], v[8:9], 0, v[52:53]
	v_add_co_u32_e32 v62, vcc, s3, v66
	v_lshlrev_b32_e32 v20, 16, v14
	v_and_b32_e32 v21, 0xffff0000, v14
	v_lshlrev_b32_e32 v14, 16, v15
	v_and_b32_e32 v15, 0xffff0000, v15
	v_pk_add_f32 v[14:15], v[18:19], v[14:15]
	v_pk_add_f32 v[16:17], v[16:17], v[20:21]
	v_and_b32_sdwa v20, v15, v88 dst_sel:DWORD dst_unused:UNUSED_PAD src0_sel:WORD_1 src1_sel:DWORD
	v_and_b32_sdwa v19, v16, v88 dst_sel:DWORD dst_unused:UNUSED_PAD src0_sel:WORD_1 src1_sel:DWORD
	v_and_b32_sdwa v21, v17, v88 dst_sel:DWORD dst_unused:UNUSED_PAD src0_sel:WORD_1 src1_sel:DWORD
	v_and_b32_sdwa v18, v14, v88 dst_sel:DWORD dst_unused:UNUSED_PAD src0_sel:WORD_1 src1_sel:DWORD
	v_add3_u32 v22, v16, v19, s22
	v_add3_u32 v19, v15, v20, s22
	v_add3_u32 v20, v17, v21, s22
	v_add3_u32 v18, v14, v18, s22
	v_and_b32_e32 v19, 0xffff0000, v19
	v_and_b32_e32 v20, 0xffff0000, v20
	v_or_b32_sdwa v19, v19, v18 dst_sel:DWORD dst_unused:UNUSED_PAD src0_sel:DWORD src1_sel:WORD_1
	v_or_b32_sdwa v18, v20, v22 dst_sel:DWORD dst_unused:UNUSED_PAD src0_sel:DWORD src1_sel:WORD_1
	global_store_dwordx2 v[46:47], v[18:19], off
	global_load_dwordx4 v[210:213], v[246:247], off
	s_nop 0
	s_waitcnt vmcnt(8)
	v_mov_b32_e32 v18, v180
	v_mov_b32_e32 v19, v181
	v_mov_b32_e32 v20, v214
	v_mov_b32_e32 v21, v215
	v_mov_b32_e32 v22, v216
	v_mov_b32_e32 v23, v217
	v_addc_co_u32_e32 v63, vcc, 0, v67, vcc
	v_add_co_u32_e32 v44, vcc, s23, v66
	v_lshlrev_b32_e32 v24, 16, v18
	v_and_b32_e32 v25, 0xffff0000, v18
	v_lshlrev_b32_e32 v18, 16, v19
	v_and_b32_e32 v19, 0xffff0000, v19
	v_pk_add_f32 v[18:19], v[22:23], v[18:19]
	v_pk_add_f32 v[20:21], v[20:21], v[24:25]
	v_and_b32_sdwa v24, v19, v88 dst_sel:DWORD dst_unused:UNUSED_PAD src0_sel:WORD_1 src1_sel:DWORD
	v_and_b32_sdwa v23, v20, v88 dst_sel:DWORD dst_unused:UNUSED_PAD src0_sel:WORD_1 src1_sel:DWORD
	v_and_b32_sdwa v25, v21, v88 dst_sel:DWORD dst_unused:UNUSED_PAD src0_sel:WORD_1 src1_sel:DWORD
	v_and_b32_sdwa v22, v18, v88 dst_sel:DWORD dst_unused:UNUSED_PAD src0_sel:WORD_1 src1_sel:DWORD
	v_add3_u32 v26, v20, v23, s22
	v_add3_u32 v23, v19, v24, s22
	v_add3_u32 v24, v21, v25, s22
	v_add3_u32 v22, v18, v22, s22
	v_and_b32_e32 v23, 0xffff0000, v23
	v_and_b32_e32 v24, 0xffff0000, v24
	v_or_b32_sdwa v23, v23, v22 dst_sel:DWORD dst_unused:UNUSED_PAD src0_sel:DWORD src1_sel:WORD_1
	v_or_b32_sdwa v22, v24, v26 dst_sel:DWORD dst_unused:UNUSED_PAD src0_sel:DWORD src1_sel:WORD_1
	global_store_dwordx2 v[46:47], v[22:23], off offset:512
	global_load_dwordx4 v[214:217], v[246:247], off offset:1024
	s_nop 0
	s_waitcnt vmcnt(9)
	v_mov_b32_e32 v22, v182
	v_mov_b32_e32 v23, v183
	v_mov_b32_e32 v24, v218
	v_mov_b32_e32 v25, v219
	v_mov_b32_e32 v26, v220
	v_mov_b32_e32 v27, v221
	v_addc_co_u32_e32 v45, vcc, 0, v67, vcc
	v_add_co_u32_e32 v74, vcc, s23, v42
	v_lshlrev_b32_e32 v28, 16, v22
	v_and_b32_e32 v29, 0xffff0000, v22
	v_lshlrev_b32_e32 v22, 16, v23
	v_and_b32_e32 v23, 0xffff0000, v23
	v_pk_add_f32 v[22:23], v[26:27], v[22:23]
	v_pk_add_f32 v[24:25], v[24:25], v[28:29]
	v_and_b32_sdwa v28, v23, v88 dst_sel:DWORD dst_unused:UNUSED_PAD src0_sel:WORD_1 src1_sel:DWORD
	v_and_b32_sdwa v27, v24, v88 dst_sel:DWORD dst_unused:UNUSED_PAD src0_sel:WORD_1 src1_sel:DWORD
	v_and_b32_sdwa v29, v25, v88 dst_sel:DWORD dst_unused:UNUSED_PAD src0_sel:WORD_1 src1_sel:DWORD
	v_and_b32_sdwa v26, v22, v88 dst_sel:DWORD dst_unused:UNUSED_PAD src0_sel:WORD_1 src1_sel:DWORD
	v_add3_u32 v30, v24, v27, s22
	v_add3_u32 v27, v23, v28, s22
	v_add3_u32 v28, v25, v29, s22
	v_add3_u32 v26, v22, v26, s22
	v_and_b32_e32 v27, 0xffff0000, v27
	v_and_b32_e32 v28, 0xffff0000, v28
	v_or_b32_sdwa v27, v27, v26 dst_sel:DWORD dst_unused:UNUSED_PAD src0_sel:DWORD src1_sel:WORD_1
	v_or_b32_sdwa v26, v28, v30 dst_sel:DWORD dst_unused:UNUSED_PAD src0_sel:DWORD src1_sel:WORD_1
	global_store_dwordx2 v[46:47], v[26:27], off offset:1024
	global_load_dwordx4 v[218:221], v[246:247], off offset:2048
	s_nop 0
	s_waitcnt vmcnt(10)
	v_mov_b32_e32 v26, v184
	v_mov_b32_e32 v27, v185
	v_mov_b32_e32 v28, v222
	v_mov_b32_e32 v29, v223
	v_mov_b32_e32 v30, v224
	v_mov_b32_e32 v31, v225
	v_addc_co_u32_e32 v75, vcc, 0, v43, vcc
	v_add_co_u32_e32 v56, vcc, s23, v46
	v_lshlrev_b32_e32 v32, 16, v26
	v_and_b32_e32 v33, 0xffff0000, v26
	v_lshlrev_b32_e32 v26, 16, v27
	v_and_b32_e32 v27, 0xffff0000, v27
	v_pk_add_f32 v[26:27], v[30:31], v[26:27]
	v_pk_add_f32 v[28:29], v[28:29], v[32:33]
	v_and_b32_sdwa v32, v27, v88 dst_sel:DWORD dst_unused:UNUSED_PAD src0_sel:WORD_1 src1_sel:DWORD
	v_and_b32_sdwa v31, v28, v88 dst_sel:DWORD dst_unused:UNUSED_PAD src0_sel:WORD_1 src1_sel:DWORD
	v_and_b32_sdwa v33, v29, v88 dst_sel:DWORD dst_unused:UNUSED_PAD src0_sel:WORD_1 src1_sel:DWORD
	v_and_b32_sdwa v30, v26, v88 dst_sel:DWORD dst_unused:UNUSED_PAD src0_sel:WORD_1 src1_sel:DWORD
	v_add3_u32 v34, v28, v31, s22
	v_add3_u32 v31, v27, v32, s22
	v_add3_u32 v32, v29, v33, s22
	v_add3_u32 v30, v26, v30, s22
	v_and_b32_e32 v31, 0xffff0000, v31
	v_and_b32_e32 v32, 0xffff0000, v32
	v_or_b32_sdwa v31, v31, v30 dst_sel:DWORD dst_unused:UNUSED_PAD src0_sel:DWORD src1_sel:WORD_1
	v_or_b32_sdwa v30, v32, v34 dst_sel:DWORD dst_unused:UNUSED_PAD src0_sel:DWORD src1_sel:WORD_1
	global_store_dwordx2 v[46:47], v[30:31], off offset:1536
	global_load_dwordx4 v[222:225], v[246:247], off offset:3072
	s_waitcnt vmcnt(11)
	v_mov_b32_e32 v34, v186
	v_mov_b32_e32 v35, v187
	v_mov_b32_e32 v30, v226
	v_mov_b32_e32 v31, v227
	v_mov_b32_e32 v32, v228
	v_mov_b32_e32 v33, v229
	v_addc_co_u32_e32 v57, vcc, 0, v47, vcc
	v_add_co_u32_e32 v82, vcc, s24, v66
	v_lshlrev_b32_e32 v36, 16, v34
	v_and_b32_e32 v37, 0xffff0000, v34
	v_lshlrev_b32_e32 v34, 16, v35
	v_and_b32_e32 v35, 0xffff0000, v35
	v_pk_add_f32 v[30:31], v[30:31], v[36:37]
	v_pk_add_f32 v[32:33], v[32:33], v[34:35]
	v_and_b32_sdwa v35, v30, v88 dst_sel:DWORD dst_unused:UNUSED_PAD src0_sel:WORD_1 src1_sel:DWORD
	v_and_b32_sdwa v36, v33, v88 dst_sel:DWORD dst_unused:UNUSED_PAD src0_sel:WORD_1 src1_sel:DWORD
	v_and_b32_sdwa v37, v31, v88 dst_sel:DWORD dst_unused:UNUSED_PAD src0_sel:WORD_1 src1_sel:DWORD
	v_and_b32_sdwa v34, v32, v88 dst_sel:DWORD dst_unused:UNUSED_PAD src0_sel:WORD_1 src1_sel:DWORD
	v_add3_u32 v38, v30, v35, s22
	v_add3_u32 v35, v33, v36, s22
	v_add3_u32 v36, v31, v37, s22
	v_add3_u32 v34, v32, v34, s22
	v_and_b32_e32 v35, 0xffff0000, v35
	v_and_b32_e32 v36, 0xffff0000, v36
	v_or_b32_sdwa v35, v35, v34 dst_sel:DWORD dst_unused:UNUSED_PAD src0_sel:DWORD src1_sel:WORD_1
	v_or_b32_sdwa v34, v36, v38 dst_sel:DWORD dst_unused:UNUSED_PAD src0_sel:DWORD src1_sel:WORD_1
	global_store_dwordx2 v[46:47], v[34:35], off offset:2048
	global_load_dwordx4 v[226:229], v[248:249], off
	v_addc_co_u32_e32 v83, vcc, 0, v67, vcc
	s_waitcnt vmcnt(12)
	v_mov_b32_e32 v38, v188
	v_mov_b32_e32 v39, v189
	v_mov_b32_e32 v34, v230
	v_mov_b32_e32 v35, v231
	v_mov_b32_e32 v36, v232
	v_mov_b32_e32 v37, v233
	v_cmp_lt_i32_e32 vcc, v157, v154
	v_lshlrev_b32_e32 v40, 16, v38
	v_and_b32_e32 v41, 0xffff0000, v38
	v_lshlrev_b32_e32 v38, 16, v39
	v_and_b32_e32 v39, 0xffff0000, v39
	v_pk_add_f32 v[34:35], v[34:35], v[40:41]
	v_pk_add_f32 v[36:37], v[36:37], v[38:39]
	v_and_b32_sdwa v39, v34, v88 dst_sel:DWORD dst_unused:UNUSED_PAD src0_sel:WORD_1 src1_sel:DWORD
	v_and_b32_sdwa v40, v37, v88 dst_sel:DWORD dst_unused:UNUSED_PAD src0_sel:WORD_1 src1_sel:DWORD
	v_and_b32_sdwa v41, v35, v88 dst_sel:DWORD dst_unused:UNUSED_PAD src0_sel:WORD_1 src1_sel:DWORD
	v_and_b32_sdwa v38, v36, v88 dst_sel:DWORD dst_unused:UNUSED_PAD src0_sel:WORD_1 src1_sel:DWORD
	v_add3_u32 v48, v34, v39, s22
	v_add3_u32 v39, v37, v40, s22
	v_add3_u32 v40, v35, v41, s22
	v_add3_u32 v38, v36, v38, s22
	v_and_b32_e32 v39, 0xffff0000, v39
	v_and_b32_e32 v40, 0xffff0000, v40
	v_or_b32_sdwa v39, v39, v38 dst_sel:DWORD dst_unused:UNUSED_PAD src0_sel:DWORD src1_sel:WORD_1
	v_or_b32_sdwa v38, v40, v48 dst_sel:DWORD dst_unused:UNUSED_PAD src0_sel:DWORD src1_sel:WORD_1
	global_store_dwordx2 v[46:47], v[38:39], off offset:2560
	global_load_dwordx4 v[230:233], v[248:249], off offset:1024
	s_nop 0
	s_waitcnt vmcnt(13)
	v_mov_b32_e32 v38, v190
	v_mov_b32_e32 v39, v191
	v_mov_b32_e32 v48, v234
	v_mov_b32_e32 v49, v235
	v_mov_b32_e32 v50, v236
	v_mov_b32_e32 v51, v237
	v_lshlrev_b32_e32 v40, 16, v38
	v_and_b32_e32 v41, 0xffff0000, v38
	v_lshlrev_b32_e32 v38, 16, v39
	v_and_b32_e32 v39, 0xffff0000, v39
	v_pk_add_f32 v[38:39], v[50:51], v[38:39]
	v_pk_add_f32 v[40:41], v[48:49], v[40:41]
	v_and_b32_sdwa v50, v39, v88 dst_sel:DWORD dst_unused:UNUSED_PAD src0_sel:WORD_1 src1_sel:DWORD
	v_and_b32_sdwa v49, v40, v88 dst_sel:DWORD dst_unused:UNUSED_PAD src0_sel:WORD_1 src1_sel:DWORD
	v_and_b32_sdwa v51, v41, v88 dst_sel:DWORD dst_unused:UNUSED_PAD src0_sel:WORD_1 src1_sel:DWORD
	v_and_b32_sdwa v48, v38, v88 dst_sel:DWORD dst_unused:UNUSED_PAD src0_sel:WORD_1 src1_sel:DWORD
	v_add3_u32 v54, v40, v49, s22
	v_add3_u32 v49, v39, v50, s22
	v_add3_u32 v50, v41, v51, s22
	v_add3_u32 v48, v38, v48, s22
	v_and_b32_e32 v49, 0xffff0000, v49
	v_and_b32_e32 v50, 0xffff0000, v50
	v_or_b32_sdwa v49, v49, v48 dst_sel:DWORD dst_unused:UNUSED_PAD src0_sel:DWORD src1_sel:WORD_1
	v_or_b32_sdwa v48, v50, v54 dst_sel:DWORD dst_unused:UNUSED_PAD src0_sel:DWORD src1_sel:WORD_1
	global_store_dwordx2 v[46:47], v[48:49], off offset:3072
	global_load_dwordx4 v[234:237], v[248:249], off offset:2048
	s_nop 0
	s_waitcnt vmcnt(14)
	v_mov_b32_e32 v54, v192
	v_mov_b32_e32 v55, v193
	v_mov_b32_e32 v48, v238
	v_mov_b32_e32 v49, v239
	v_mov_b32_e32 v50, v240
	v_mov_b32_e32 v51, v241
	v_mul_f32_e32 v102, v39, v39
	v_lshlrev_b32_e32 v42, 16, v54
	v_and_b32_e32 v43, 0xffff0000, v54
	v_lshlrev_b32_e32 v44, 16, v55
	v_and_b32_e32 v45, 0xffff0000, v55
	v_pk_add_f32 v[42:43], v[48:49], v[42:43]
	v_pk_add_f32 v[44:45], v[50:51], v[44:45]
	v_and_b32_sdwa v49, v42, v88 dst_sel:DWORD dst_unused:UNUSED_PAD src0_sel:WORD_1 src1_sel:DWORD
	v_and_b32_sdwa v50, v45, v88 dst_sel:DWORD dst_unused:UNUSED_PAD src0_sel:WORD_1 src1_sel:DWORD
	v_and_b32_sdwa v51, v43, v88 dst_sel:DWORD dst_unused:UNUSED_PAD src0_sel:WORD_1 src1_sel:DWORD
	v_and_b32_sdwa v48, v44, v88 dst_sel:DWORD dst_unused:UNUSED_PAD src0_sel:WORD_1 src1_sel:DWORD
	v_add3_u32 v54, v42, v49, s22
	v_add3_u32 v49, v45, v50, s22
	v_add3_u32 v50, v43, v51, s22
	v_add3_u32 v48, v44, v48, s22
	v_and_b32_e32 v49, 0xffff0000, v49
	v_and_b32_e32 v50, 0xffff0000, v50
	v_or_b32_sdwa v49, v49, v48 dst_sel:DWORD dst_unused:UNUSED_PAD src0_sel:DWORD src1_sel:WORD_1
	v_or_b32_sdwa v48, v50, v54 dst_sel:DWORD dst_unused:UNUSED_PAD src0_sel:DWORD src1_sel:WORD_1
	global_store_dwordx2 v[46:47], v[48:49], off offset:3584
	global_load_dwordx4 v[238:241], v[248:249], off offset:3072
	s_waitcnt vmcnt(14)
	v_mov_b32_e32 v54, v194
	v_mov_b32_e32 v55, v195
	v_mov_b32_e32 v48, v210
	v_mov_b32_e32 v49, v211
	v_mov_b32_e32 v50, v212
	v_mov_b32_e32 v51, v213
	v_lshlrev_b32_e32 v58, 16, v54
	v_and_b32_e32 v59, 0xffff0000, v54
	v_lshlrev_b32_e32 v46, 16, v55
	v_and_b32_e32 v47, 0xffff0000, v55
	v_pk_add_f32 v[46:47], v[50:51], v[46:47]
	v_pk_add_f32 v[48:49], v[48:49], v[58:59]
	v_and_b32_sdwa v54, v47, v88 dst_sel:DWORD dst_unused:UNUSED_PAD src0_sel:WORD_1 src1_sel:DWORD
	v_and_b32_sdwa v51, v48, v88 dst_sel:DWORD dst_unused:UNUSED_PAD src0_sel:WORD_1 src1_sel:DWORD
	v_and_b32_sdwa v55, v49, v88 dst_sel:DWORD dst_unused:UNUSED_PAD src0_sel:WORD_1 src1_sel:DWORD
	v_and_b32_sdwa v50, v46, v88 dst_sel:DWORD dst_unused:UNUSED_PAD src0_sel:WORD_1 src1_sel:DWORD
	v_add3_u32 v58, v48, v51, s22
	v_add3_u32 v51, v47, v54, s22
	v_add3_u32 v54, v49, v55, s22
	v_add3_u32 v50, v46, v50, s22
	v_and_b32_e32 v51, 0xffff0000, v51
	v_and_b32_e32 v54, 0xffff0000, v54
	v_or_b32_sdwa v51, v51, v50 dst_sel:DWORD dst_unused:UNUSED_PAD src0_sel:DWORD src1_sel:WORD_1
	v_or_b32_sdwa v50, v54, v58 dst_sel:DWORD dst_unused:UNUSED_PAD src0_sel:DWORD src1_sel:WORD_1
	global_store_dwordx2 v[56:57], v[50:51], off
	s_nop 0
	s_waitcnt vmcnt(13)
	v_mov_b32_e32 v50, v196
	v_mov_b32_e32 v51, v197
	v_mov_b32_e32 v58, v214
	v_mov_b32_e32 v59, v215
	v_mov_b32_e32 v60, v216
	v_mov_b32_e32 v61, v217
	v_lshlrev_b32_e32 v54, 16, v50
	v_and_b32_e32 v55, 0xffff0000, v50
	v_lshlrev_b32_e32 v50, 16, v51
	v_and_b32_e32 v51, 0xffff0000, v51
	v_pk_add_f32 v[50:51], v[60:61], v[50:51]
	v_pk_add_f32 v[54:55], v[58:59], v[54:55]
	v_and_b32_sdwa v60, v51, v88 dst_sel:DWORD dst_unused:UNUSED_PAD src0_sel:WORD_1 src1_sel:DWORD
	v_and_b32_sdwa v59, v54, v88 dst_sel:DWORD dst_unused:UNUSED_PAD src0_sel:WORD_1 src1_sel:DWORD
	v_and_b32_sdwa v61, v55, v88 dst_sel:DWORD dst_unused:UNUSED_PAD src0_sel:WORD_1 src1_sel:DWORD
	v_and_b32_sdwa v58, v50, v88 dst_sel:DWORD dst_unused:UNUSED_PAD src0_sel:WORD_1 src1_sel:DWORD
	v_add3_u32 v64, v54, v59, s22
	v_add3_u32 v59, v51, v60, s22
	v_add3_u32 v60, v55, v61, s22
	v_add3_u32 v58, v50, v58, s22
	v_and_b32_e32 v59, 0xffff0000, v59
	v_and_b32_e32 v60, 0xffff0000, v60
	v_or_b32_sdwa v59, v59, v58 dst_sel:DWORD dst_unused:UNUSED_PAD src0_sel:DWORD src1_sel:WORD_1
	v_or_b32_sdwa v58, v60, v64 dst_sel:DWORD dst_unused:UNUSED_PAD src0_sel:DWORD src1_sel:WORD_1
	global_store_dwordx2 v[56:57], v[58:59], off offset:512
	s_nop 0
	s_waitcnt vmcnt(12)
	v_mov_b32_e32 v58, v198
	v_mov_b32_e32 v59, v199
	v_mov_b32_e32 v68, v218
	v_mov_b32_e32 v69, v219
	v_mov_b32_e32 v70, v220
	v_mov_b32_e32 v71, v221
	v_lshlrev_b32_e32 v60, 16, v58
	v_and_b32_e32 v61, 0xffff0000, v58
	v_lshlrev_b32_e32 v58, 16, v59
	v_and_b32_e32 v59, 0xffff0000, v59
	v_pk_add_f32 v[58:59], v[70:71], v[58:59]
	v_pk_add_f32 v[60:61], v[68:69], v[60:61]
	v_and_b32_sdwa v68, v59, v88 dst_sel:DWORD dst_unused:UNUSED_PAD src0_sel:WORD_1 src1_sel:DWORD
	v_and_b32_sdwa v65, v60, v88 dst_sel:DWORD dst_unused:UNUSED_PAD src0_sel:WORD_1 src1_sel:DWORD
	v_and_b32_sdwa v69, v61, v88 dst_sel:DWORD dst_unused:UNUSED_PAD src0_sel:WORD_1 src1_sel:DWORD
	v_and_b32_sdwa v64, v58, v88 dst_sel:DWORD dst_unused:UNUSED_PAD src0_sel:WORD_1 src1_sel:DWORD
	v_add3_u32 v70, v60, v65, s22
	v_add3_u32 v65, v59, v68, s22
	v_add3_u32 v68, v61, v69, s22
	v_add3_u32 v64, v58, v64, s22
	v_and_b32_e32 v65, 0xffff0000, v65
	v_and_b32_e32 v68, 0xffff0000, v68
	v_or_b32_sdwa v65, v65, v64 dst_sel:DWORD dst_unused:UNUSED_PAD src0_sel:DWORD src1_sel:WORD_1
	v_or_b32_sdwa v64, v68, v70 dst_sel:DWORD dst_unused:UNUSED_PAD src0_sel:DWORD src1_sel:WORD_1
	global_store_dwordx2 v[56:57], v[64:65], off offset:1024
	s_nop 0
	s_waitcnt vmcnt(11)
	v_mov_b32_e32 v64, v200
	v_mov_b32_e32 v65, v201
	v_mov_b32_e32 v68, v222
	v_mov_b32_e32 v69, v223
	v_mov_b32_e32 v70, v224
	v_mov_b32_e32 v71, v225
	v_lshlrev_b32_e32 v72, 16, v64
	v_and_b32_e32 v73, 0xffff0000, v64
	v_lshlrev_b32_e32 v62, 16, v65
	v_and_b32_e32 v63, 0xffff0000, v65
	v_pk_add_f32 v[62:63], v[70:71], v[62:63]
	v_pk_add_f32 v[64:65], v[68:69], v[72:73]
	v_and_b32_sdwa v70, v63, v88 dst_sel:DWORD dst_unused:UNUSED_PAD src0_sel:WORD_1 src1_sel:DWORD
	v_and_b32_sdwa v69, v64, v88 dst_sel:DWORD dst_unused:UNUSED_PAD src0_sel:WORD_1 src1_sel:DWORD
	v_and_b32_sdwa v71, v65, v88 dst_sel:DWORD dst_unused:UNUSED_PAD src0_sel:WORD_1 src1_sel:DWORD
	v_and_b32_sdwa v68, v62, v88 dst_sel:DWORD dst_unused:UNUSED_PAD src0_sel:WORD_1 src1_sel:DWORD
	v_add3_u32 v72, v64, v69, s22
	v_add3_u32 v69, v63, v70, s22
	v_add3_u32 v70, v65, v71, s22
	v_add3_u32 v68, v62, v68, s22
	v_and_b32_e32 v69, 0xffff0000, v69
	v_and_b32_e32 v70, 0xffff0000, v70
	v_or_b32_sdwa v69, v69, v68 dst_sel:DWORD dst_unused:UNUSED_PAD src0_sel:DWORD src1_sel:WORD_1
	v_or_b32_sdwa v68, v70, v72 dst_sel:DWORD dst_unused:UNUSED_PAD src0_sel:DWORD src1_sel:WORD_1
	global_store_dwordx2 v[56:57], v[68:69], off offset:1536
	s_waitcnt vmcnt(10)
	v_mov_b32_e32 v72, v202
	v_mov_b32_e32 v73, v203
	v_mov_b32_e32 v68, v226
	v_mov_b32_e32 v69, v227
	v_mov_b32_e32 v70, v228
	v_mov_b32_e32 v71, v229
	v_lshlrev_b32_e32 v76, 16, v72
	v_and_b32_e32 v77, 0xffff0000, v72
	v_lshlrev_b32_e32 v66, 16, v73
	v_and_b32_e32 v67, 0xffff0000, v73
	v_pk_add_f32 v[66:67], v[70:71], v[66:67]
	v_pk_add_f32 v[68:69], v[68:69], v[76:77]
	v_and_b32_sdwa v72, v67, v88 dst_sel:DWORD dst_unused:UNUSED_PAD src0_sel:WORD_1 src1_sel:DWORD
	v_and_b32_sdwa v71, v68, v88 dst_sel:DWORD dst_unused:UNUSED_PAD src0_sel:WORD_1 src1_sel:DWORD
	v_and_b32_sdwa v73, v69, v88 dst_sel:DWORD dst_unused:UNUSED_PAD src0_sel:WORD_1 src1_sel:DWORD
	v_and_b32_sdwa v70, v66, v88 dst_sel:DWORD dst_unused:UNUSED_PAD src0_sel:WORD_1 src1_sel:DWORD
	v_add3_u32 v76, v68, v71, s22
	v_add3_u32 v71, v67, v72, s22
	v_add3_u32 v72, v69, v73, s22
	v_add3_u32 v70, v66, v70, s22
	v_and_b32_e32 v71, 0xffff0000, v71
	v_and_b32_e32 v72, 0xffff0000, v72
	v_or_b32_sdwa v71, v71, v70 dst_sel:DWORD dst_unused:UNUSED_PAD src0_sel:DWORD src1_sel:WORD_1
	v_or_b32_sdwa v70, v72, v76 dst_sel:DWORD dst_unused:UNUSED_PAD src0_sel:DWORD src1_sel:WORD_1
	global_store_dwordx2 v[56:57], v[70:71], off offset:2048
	s_nop 0
	s_waitcnt vmcnt(9)
	v_mov_b32_e32 v70, v204
	v_mov_b32_e32 v71, v205
	v_mov_b32_e32 v76, v230
	v_mov_b32_e32 v77, v231
	v_mov_b32_e32 v78, v232
	v_mov_b32_e32 v79, v233
	v_lshlrev_b32_e32 v72, 16, v70
	v_and_b32_e32 v73, 0xffff0000, v70
	v_lshlrev_b32_e32 v70, 16, v71
	v_and_b32_e32 v71, 0xffff0000, v71
	v_pk_add_f32 v[70:71], v[78:79], v[70:71]
	v_pk_add_f32 v[72:73], v[76:77], v[72:73]
	v_and_b32_sdwa v78, v71, v88 dst_sel:DWORD dst_unused:UNUSED_PAD src0_sel:WORD_1 src1_sel:DWORD
	v_and_b32_sdwa v77, v72, v88 dst_sel:DWORD dst_unused:UNUSED_PAD src0_sel:WORD_1 src1_sel:DWORD
	v_and_b32_sdwa v79, v73, v88 dst_sel:DWORD dst_unused:UNUSED_PAD src0_sel:WORD_1 src1_sel:DWORD
	v_and_b32_sdwa v76, v70, v88 dst_sel:DWORD dst_unused:UNUSED_PAD src0_sel:WORD_1 src1_sel:DWORD
	v_add3_u32 v80, v72, v77, s22
	v_add3_u32 v77, v71, v78, s22
	v_add3_u32 v78, v73, v79, s22
	v_add3_u32 v76, v70, v76, s22
	v_and_b32_e32 v77, 0xffff0000, v77
	v_and_b32_e32 v78, 0xffff0000, v78
	v_or_b32_sdwa v77, v77, v76 dst_sel:DWORD dst_unused:UNUSED_PAD src0_sel:DWORD src1_sel:WORD_1
	v_or_b32_sdwa v76, v78, v80 dst_sel:DWORD dst_unused:UNUSED_PAD src0_sel:DWORD src1_sel:WORD_1
	global_store_dwordx2 v[56:57], v[76:77], off offset:2560
	s_nop 0
	s_waitcnt vmcnt(8)
	v_mov_b32_e32 v76, v206
	v_mov_b32_e32 v77, v207
	v_mov_b32_e32 v94, v234
	v_mov_b32_e32 v95, v235
	v_mov_b32_e32 v96, v236
	v_mov_b32_e32 v97, v237
	v_cndmask_b32_e32 v78, v1, v157, vcc
	v_cmp_lt_i32_e32 vcc, v158, v154
	v_lshlrev_b32_e32 v92, 2, v78
	v_lshlrev_b64 v[80:81], 12, v[2:3]
	v_cndmask_b32_e32 v79, v1, v158, vcc
	v_cmp_lt_i32_e32 vcc, v159, v154
	v_lshlrev_b32_e32 v91, 2, v79
	v_pk_mul_f32 v[78:79], v[14:15], v[14:15]
	v_cndmask_b32_e32 v84, v1, v159, vcc
	v_cmp_lt_i32_e32 vcc, v160, v154
	v_lshlrev_b32_e32 v90, 2, v84
	s_nop 0
	v_cndmask_b32_e32 v85, v1, v160, vcc
	v_lshlrev_b32_e32 v89, 2, v85
	v_pk_mul_f32 v[84:85], v[16:17], v[16:17]
	v_cmp_lt_i32_e32 vcc, v156, v154
	v_pk_mov_b32 v[98:99], v[84:85], v[78:79] op_sel:[1,0]
	v_mov_b32_e32 v85, v79
	v_pk_add_f32 v[78:79], v[98:99], v[84:85]
	v_pk_mul_f32 v[84:85], v[18:19], v[18:19]
	v_pk_mul_f32 v[98:99], v[20:21], v[20:21]
	v_pk_add_f32 v[78:79], v[78:79], v[78:79] op_sel:[0,1] op_sel_hi:[1,0]
	v_pk_mov_b32 v[100:101], v[98:99], v[84:85] op_sel:[1,0]
	v_mov_b32_e32 v99, v85
	v_pk_add_f32 v[84:85], v[100:101], v[98:99]
	v_mul_f32_e32 v79, v28, v28
	v_pk_add_f32 v[84:85], v[84:85], v[84:85] op_sel:[0,1] op_sel_hi:[1,0]
	v_mul_f32_e32 v98, v25, v25
	v_mul_f32_e32 v85, v29, v29
	v_mul_f32_e32 v100, v23, v23
	v_pk_add_f32 v[84:85], v[78:79], v[84:85]
	v_pk_fma_f32 v[98:99], v[24:25], v[24:25], v[98:99] op_sel_hi:[1,1,0]
	v_pk_fma_f32 v[100:101], v[22:23], v[22:23], v[100:101] op_sel_hi:[1,1,0]
	v_mul_f32_e32 v99, v26, v26
	v_mul_f32_e32 v101, v27, v27
	v_pk_add_f32 v[98:99], v[98:99], v[100:101]
	v_cndmask_b32_e32 v93, v1, v156, vcc
	v_pk_add_f32 v[84:85], v[84:85], v[98:99]
	v_pk_mul_f32 v[98:99], v[32:33], v[32:33]
	v_pk_add_f32 v[84:85], v[84:85], v[84:85] op_sel:[0,1] op_sel_hi:[1,0]
	v_cmp_lt_i32_e32 vcc, v155, v154
	v_mul_f32_e32 v85, v40, v40
	v_lshlrev_b32_e32 v78, 16, v76
	v_and_b32_e32 v79, 0xffff0000, v76
	v_lshlrev_b32_e32 v76, 16, v77
	v_and_b32_e32 v77, 0xffff0000, v77
	v_pk_add_f32 v[76:77], v[96:97], v[76:77]
	v_pk_add_f32 v[78:79], v[94:95], v[78:79]
	v_and_b32_sdwa v96, v77, v88 dst_sel:DWORD dst_unused:UNUSED_PAD src0_sel:WORD_1 src1_sel:DWORD
	v_and_b32_sdwa v95, v78, v88 dst_sel:DWORD dst_unused:UNUSED_PAD src0_sel:WORD_1 src1_sel:DWORD
	v_and_b32_sdwa v97, v79, v88 dst_sel:DWORD dst_unused:UNUSED_PAD src0_sel:WORD_1 src1_sel:DWORD
	v_and_b32_sdwa v94, v76, v88 dst_sel:DWORD dst_unused:UNUSED_PAD src0_sel:WORD_1 src1_sel:DWORD
	v_add3_u32 v100, v78, v95, s22
	v_add3_u32 v95, v77, v96, s22
	v_add3_u32 v96, v79, v97, s22
	v_add3_u32 v94, v76, v94, s22
	v_and_b32_e32 v95, 0xffff0000, v95
	v_and_b32_e32 v96, 0xffff0000, v96
	v_or_b32_sdwa v95, v95, v94 dst_sel:DWORD dst_unused:UNUSED_PAD src0_sel:DWORD src1_sel:WORD_1
	v_or_b32_sdwa v94, v96, v100 dst_sel:DWORD dst_unused:UNUSED_PAD src0_sel:DWORD src1_sel:WORD_1
	global_store_dwordx2 v[56:57], v[94:95], off offset:3072
	v_cndmask_b32_e32 v106, v1, v155, vcc
	s_waitcnt vmcnt(7)
	v_mov_b32_e32 v74, v208
	v_mov_b32_e32 v75, v209
	v_mov_b32_e32 v94, v238
	v_mov_b32_e32 v95, v239
	v_mov_b32_e32 v96, v240
	v_mov_b32_e32 v97, v241
	v_pk_mul_f32 v[82:83], v[30:31], v[30:31]
	s_nop 0
	v_pk_mov_b32 v[100:101], v[82:83], v[98:99] op_sel:[1,0]
	v_mov_b32_e32 v83, v99
	v_pk_add_f32 v[82:83], v[100:101], v[82:83]
	v_mul_f32_e32 v98, v35, v35
	v_mul_f32_e32 v100, v37, v37
	v_pk_fma_f32 v[98:99], v[34:35], v[34:35], v[98:99] op_sel_hi:[1,1,0]
	v_pk_fma_f32 v[100:101], v[36:37], v[36:37], v[100:101] op_sel_hi:[1,1,0]
	v_pk_add_f32 v[82:83], v[82:83], v[82:83] op_sel:[0,1] op_sel_hi:[1,0]
	v_mul_f32_e32 v99, v41, v41
	v_mul_f32_e32 v101, v38, v38
	v_mov_b32_e32 v83, v99
	v_mov_b32_e32 v99, v101
	v_mov_b32_e32 v101, v102
	v_pk_add_f32 v[82:83], v[84:85], v[82:83]
	v_pk_add_f32 v[84:85], v[98:99], v[100:101]
	v_pk_mul_f32 v[98:99], v[42:43], v[42:43]
	v_pk_add_f32 v[82:83], v[82:83], v[84:85]
	v_pk_mul_f32 v[84:85], v[44:45], v[44:45]
	v_pk_add_f32 v[82:83], v[82:83], v[82:83] op_sel:[0,1] op_sel_hi:[1,0]
	v_pk_mov_b32 v[100:101], v[98:99], v[84:85] op_sel:[1,0]
	v_mov_b32_e32 v99, v85
	v_pk_add_f32 v[84:85], v[100:101], v[98:99]
	v_mul_f32_e32 v98, v49, v49
	v_mul_f32_e32 v100, v47, v47
	v_pk_add_f32 v[84:85], v[84:85], v[84:85] op_sel:[0,1] op_sel_hi:[1,0]
	v_pk_fma_f32 v[98:99], v[48:49], v[48:49], v[98:99] op_sel_hi:[1,1,0]
	v_pk_fma_f32 v[100:101], v[46:47], v[46:47], v[100:101] op_sel_hi:[1,1,0]
	v_mul_f32_e32 v83, v54, v54
	v_mul_f32_e32 v85, v55, v55
	v_mul_f32_e32 v99, v50, v50
	v_mul_f32_e32 v101, v51, v51
	v_pk_add_f32 v[82:83], v[82:83], v[84:85]
	v_pk_add_f32 v[84:85], v[98:99], v[100:101]
	v_pk_mul_f32 v[98:99], v[60:61], v[60:61]
	v_pk_add_f32 v[82:83], v[82:83], v[84:85]
	v_pk_mul_f32 v[84:85], v[58:59], v[58:59]
	v_pk_add_f32 v[82:83], v[82:83], v[82:83] op_sel:[0,1] op_sel_hi:[1,0]
	v_pk_mov_b32 v[100:101], v[98:99], v[84:85] op_sel:[1,0]
	v_mov_b32_e32 v99, v85
	v_pk_add_f32 v[84:85], v[100:101], v[98:99]
	v_mul_f32_e32 v98, v65, v65
	v_mul_f32_e32 v100, v63, v63
	v_pk_add_f32 v[84:85], v[84:85], v[84:85] op_sel:[0,1] op_sel_hi:[1,0]
	v_pk_fma_f32 v[98:99], v[64:65], v[64:65], v[98:99] op_sel_hi:[1,1,0]
	v_pk_fma_f32 v[100:101], v[62:63], v[62:63], v[100:101] op_sel_hi:[1,1,0]
	v_mul_f32_e32 v83, v68, v68
	v_mul_f32_e32 v85, v69, v69
	v_mul_f32_e32 v99, v66, v66
	v_mul_f32_e32 v101, v67, v67
	v_pk_add_f32 v[82:83], v[82:83], v[84:85]
	v_pk_add_f32 v[84:85], v[98:99], v[100:101]
	s_nop 0
	v_pk_add_f32 v[82:83], v[82:83], v[84:85]
	v_pk_mul_f32 v[84:85], v[72:73], v[72:73]
	v_pk_add_f32 v[98:99], v[82:83], v[82:83] op_sel:[0,1] op_sel_hi:[1,0]
	v_pk_mul_f32 v[82:83], v[70:71], v[70:71]
	s_nop 0
	v_pk_mov_b32 v[100:101], v[84:85], v[82:83] op_sel:[1,0]
	v_mov_b32_e32 v85, v83
	v_pk_add_f32 v[82:83], v[100:101], v[84:85]
	v_mul_f32_e32 v84, v77, v77
	v_pk_add_f32 v[100:101], v[82:83], v[82:83] op_sel:[0,1] op_sel_hi:[1,0]
	v_mul_f32_e32 v82, v79, v79
	v_pk_fma_f32 v[104:105], v[76:77], v[76:77], v[84:85] op_sel_hi:[1,1,0]
	v_pk_fma_f32 v[102:103], v[78:79], v[78:79], v[82:83] op_sel_hi:[1,1,0]
	v_lshlrev_b32_e32 v84, 16, v74
	v_and_b32_e32 v85, 0xffff0000, v74
	v_lshlrev_b32_e32 v74, 16, v75
	v_and_b32_e32 v75, 0xffff0000, v75
	v_pk_add_f32 v[82:83], v[96:97], v[74:75]
	v_pk_add_f32 v[84:85], v[94:95], v[84:85]
	v_mul_f32_e32 v103, v82, v82
	v_mul_f32_e32 v99, v84, v84
	v_mul_f32_e32 v101, v85, v85
	v_mul_f32_e32 v105, v83, v83
	v_pk_add_f32 v[74:75], v[98:99], v[100:101]
	v_pk_add_f32 v[94:95], v[102:103], v[104:105]
	v_and_b32_sdwa v99, v83, v88 dst_sel:DWORD dst_unused:UNUSED_PAD src0_sel:WORD_1 src1_sel:DWORD
	v_pk_add_f32 v[74:75], v[74:75], v[94:95]
	v_lshlrev_b32_e32 v94, 2, v93
	v_add_f32_e32 v95, v74, v75
	ds_bpermute_b32 v96, v92, v95
	v_and_b32_sdwa v100, v85, v88 dst_sel:DWORD dst_unused:UNUSED_PAD src0_sel:WORD_1 src1_sel:DWORD
	v_and_b32_sdwa v97, v82, v88 dst_sel:DWORD dst_unused:UNUSED_PAD src0_sel:WORD_1 src1_sel:DWORD
	v_and_b32_sdwa v98, v84, v88 dst_sel:DWORD dst_unused:UNUSED_PAD src0_sel:WORD_1 src1_sel:DWORD
	v_add3_u32 v99, v83, v99, s22
	s_waitcnt lgkmcnt(0)
	v_add_f32_e32 v95, v95, v96
	ds_bpermute_b32 v96, v91, v95
	v_add3_u32 v100, v85, v100, s22
	v_add3_u32 v98, v84, v98, s22
	v_add3_u32 v97, v82, v97, s22
	v_and_b32_e32 v99, 0xffff0000, v99
	s_waitcnt lgkmcnt(0)
	v_add_f32_e32 v95, v95, v96
	ds_bpermute_b32 v96, v90, v95
	v_and_b32_e32 v100, 0xffff0000, v100
	v_or_b32_sdwa v97, v99, v97 dst_sel:DWORD dst_unused:UNUSED_PAD src0_sel:DWORD src1_sel:WORD_1
	v_lshlrev_b32_e32 v93, 2, v106
	v_lshl_add_u64 v[74:75], v[10:11], 0, v[52:53]
	s_waitcnt lgkmcnt(0)
	v_add_f32_e32 v95, v95, v96
	ds_bpermute_b32 v96, v89, v95
	v_lshl_add_u64 v[52:53], v[12:13], 0, v[80:81]
	v_add_co_u32_e32 v80, vcc, s23, v74
	s_waitcnt lgkmcnt(0)
	v_add_f32_e32 v95, v95, v96
	ds_bpermute_b32 v101, v94, v95
	v_or_b32_sdwa v96, v100, v98 dst_sel:DWORD dst_unused:UNUSED_PAD src0_sel:DWORD src1_sel:WORD_1
	global_store_dwordx2 v[56:57], v[96:97], off offset:3584
	v_addc_co_u32_e32 v81, vcc, 0, v75, vcc
	s_waitcnt lgkmcnt(0)
	v_add_f32_e32 v56, v95, v101
	ds_bpermute_b32 v57, v93, v56
	ds_read_b128 v[96:99], v86 offset:16384
	ds_read_b128 v[100:103], v86 offset:17408
	ds_read_b128 v[104:107], v86
	ds_read_b128 v[108:111], v86 offset:1024
	ds_read_b128 v[112:115], v86 offset:18432
	ds_read_b128 v[116:119], v86 offset:19456
	ds_read_b128 v[120:123], v86 offset:2048
	ds_read_b128 v[124:127], v86 offset:3072
	s_waitcnt lgkmcnt(8)
	v_add_f32_e32 v56, v56, v57
	v_fmamk_f32 v56, v56, 0x39800000, v87
	v_mul_f32_e32 v57, 0x4b800000, v56
	v_cmp_gt_f32_e32 vcc, s25, v56
	s_nop 1
	v_cndmask_b32_e32 v56, v56, v57, vcc
	v_rsq_f32_e32 v56, v56
	s_nop 0
	v_mul_f32_e32 v57, 0x45800000, v56
	v_cndmask_b32_e32 v56, v56, v57, vcc
	v_pk_mul_f32 v[16:17], v[16:17], v[56:57] op_sel_hi:[1,0]
	v_pk_mul_f32 v[14:15], v[14:15], v[56:57] op_sel_hi:[1,0]
	v_pk_mul_f32 v[20:21], v[20:21], v[56:57] op_sel_hi:[1,0]
	v_pk_mul_f32 v[18:19], v[18:19], v[56:57] op_sel_hi:[1,0]
	v_pk_mul_f32 v[24:25], v[24:25], v[56:57] op_sel_hi:[1,0]
	v_pk_mul_f32 v[22:23], v[22:23], v[56:57] op_sel_hi:[1,0]
	v_pk_mul_f32 v[28:29], v[28:29], v[56:57] op_sel_hi:[1,0]
	v_pk_mul_f32 v[26:27], v[26:27], v[56:57] op_sel_hi:[1,0]
	v_pk_mul_f32 v[166:167], v[72:73], v[56:57] op_sel_hi:[1,0]
	v_pk_mul_f32 v[170:171], v[78:79], v[56:57] op_sel_hi:[1,0]
	s_waitcnt lgkmcnt(5)
	v_pk_fma_f32 v[72:73], v[106:107], v[14:15], v[98:99]
	v_pk_fma_f32 v[78:79], v[104:105], v[16:17], v[96:97]
	v_pk_mul_f32 v[128:129], v[30:31], v[56:57] op_sel_hi:[1,0]
	v_pk_mul_f32 v[130:131], v[32:33], v[56:57] op_sel_hi:[1,0]
	v_pk_mul_f32 v[34:35], v[34:35], v[56:57] op_sel_hi:[1,0]
	v_pk_mul_f32 v[36:37], v[36:37], v[56:57] op_sel_hi:[1,0]
	v_pk_mul_f32 v[132:133], v[40:41], v[56:57] op_sel_hi:[1,0]
	v_pk_mul_f32 v[134:135], v[38:39], v[56:57] op_sel_hi:[1,0]
	v_pk_mul_f32 v[136:137], v[42:43], v[56:57] op_sel_hi:[1,0]
	v_pk_mul_f32 v[138:139], v[44:45], v[56:57] op_sel_hi:[1,0]
	v_pk_mul_f32 v[140:141], v[48:49], v[56:57] op_sel_hi:[1,0]
	v_pk_mul_f32 v[142:143], v[46:47], v[56:57] op_sel_hi:[1,0]
	v_pk_mul_f32 v[54:55], v[54:55], v[56:57] op_sel_hi:[1,0]
	v_pk_mul_f32 v[144:145], v[50:51], v[56:57] op_sel_hi:[1,0]
	v_pk_mul_f32 v[146:147], v[60:61], v[56:57] op_sel_hi:[1,0]
	v_pk_mul_f32 v[148:149], v[58:59], v[56:57] op_sel_hi:[1,0]
	v_pk_mul_f32 v[150:151], v[64:65], v[56:57] op_sel_hi:[1,0]
	v_pk_mul_f32 v[152:153], v[62:63], v[56:57] op_sel_hi:[1,0]
	v_pk_mul_f32 v[162:163], v[68:69], v[56:57] op_sel_hi:[1,0]
	v_pk_mul_f32 v[164:165], v[66:67], v[56:57] op_sel_hi:[1,0]
	v_pk_mul_f32 v[168:169], v[70:71], v[56:57] op_sel_hi:[1,0]
	v_pk_mul_f32 v[172:173], v[76:77], v[56:57] op_sel_hi:[1,0]
	v_pk_mul_f32 v[174:175], v[84:85], v[56:57] op_sel_hi:[1,0]
	v_pk_mul_f32 v[176:177], v[82:83], v[56:57] op_sel_hi:[1,0]
	s_waitcnt lgkmcnt(4)
	v_pk_fma_f32 v[56:57], v[110:111], v[18:19], v[102:103]
	v_pk_fma_f32 v[62:63], v[108:109], v[20:21], v[100:101]
	s_waitcnt lgkmcnt(1)
	v_pk_fma_f32 v[38:39], v[122:123], v[22:23], v[114:115]
	v_pk_fma_f32 v[44:45], v[120:121], v[24:25], v[112:113]
	s_waitcnt lgkmcnt(0)
	v_pk_fma_f32 v[22:23], v[126:127], v[26:27], v[118:119]
	v_pk_fma_f32 v[28:29], v[124:125], v[28:29], v[116:117]
	v_bfe_u32 v14, v78, 16, 1
	v_bfe_u32 v16, v72, 16, 1
	v_bfe_u32 v15, v79, 16, 1
	v_bfe_u32 v17, v73, 16, 1
	v_bfe_u32 v18, v62, 16, 1
	v_bfe_u32 v20, v56, 16, 1
	v_bfe_u32 v24, v44, 16, 1
	v_bfe_u32 v26, v38, 16, 1
	v_bfe_u32 v30, v28, 16, 1
	v_bfe_u32 v32, v22, 16, 1
	v_add3_u32 v14, v78, v14, s22
	v_add3_u32 v16, v72, v16, s22
	v_bfe_u32 v19, v63, 16, 1
	v_bfe_u32 v21, v57, 16, 1
	v_bfe_u32 v25, v45, 16, 1
	v_bfe_u32 v27, v39, 16, 1
	v_bfe_u32 v31, v29, 16, 1
	v_bfe_u32 v33, v23, 16, 1
	v_max_f32_e64 v40, |v78|, |v79|
	v_max_f32_e64 v41, |v72|, |v73|
	v_add3_u32 v15, v79, v15, s22
	v_add3_u32 v17, v73, v17, s22
	v_add3_u32 v18, v62, v18, s22
	v_add3_u32 v20, v56, v20, s22
	v_add3_u32 v24, v44, v24, s22
	v_add3_u32 v26, v38, v26, s22
	v_add3_u32 v30, v28, v30, s22
	v_add3_u32 v32, v22, v32, s22
	v_lshrrev_b32_e32 v14, 16, v14
	v_lshrrev_b32_e32 v16, 16, v16
	v_max_f32_e64 v42, |v62|, |v63|
	v_max_f32_e64 v43, |v56|, |v57|
	v_add3_u32 v19, v63, v19, s22
	v_add3_u32 v21, v57, v21, s22
	v_add3_u32 v25, v45, v25, s22
	v_add3_u32 v27, v39, v27, s22
	v_add3_u32 v31, v29, v31, s22
	v_add3_u32 v33, v23, v33, s22
	v_max3_f32 v40, v40, 0, v41
	v_lshrrev_b32_e32 v18, 16, v18
	v_lshrrev_b32_e32 v20, 16, v20
	v_lshrrev_b32_e32 v24, 16, v24
	v_lshrrev_b32_e32 v26, 16, v26
	v_lshrrev_b32_e32 v30, 16, v30
	v_lshrrev_b32_e32 v32, 16, v32
	v_and_or_b32 v14, v15, s21, v14
	v_and_or_b32 v15, v17, s21, v16
	v_max_f32_e64 v46, |v44|, |v45|
	v_max_f32_e64 v47, |v38|, |v39|
	v_max3_f32 v40, v40, v42, v43
	v_and_or_b32 v16, v19, s21, v18
	v_and_or_b32 v17, v21, s21, v20
	v_and_or_b32 v18, v25, s21, v24
	v_and_or_b32 v19, v27, s21, v26
	v_and_or_b32 v20, v31, s21, v30
	v_and_or_b32 v21, v33, s21, v32
	global_store_dwordx2 v[74:75], v[14:15], off
	global_store_dwordx2 v[74:75], v[16:17], off offset:512
	global_store_dwordx2 v[74:75], v[18:19], off offset:1024
	global_store_dwordx2 v[74:75], v[20:21], off offset:1536
	v_max_f32_e64 v48, |v28|, |v29|
	v_max_f32_e64 v49, |v22|, |v23|
	v_max3_f32 v24, v40, v46, v47
	v_max3_f32 v58, v24, v48, v49
	ds_read_b128 v[14:17], v86 offset:20480
	ds_read_b128 v[18:21], v86 offset:21504
	ds_read_b128 v[24:27], v86 offset:4096
	ds_read_b128 v[30:33], v86 offset:5120
	ds_read_b128 v[40:43], v86 offset:22528
	ds_read_b128 v[46:49], v86 offset:23552
	ds_read_b128 v[64:67], v86 offset:6144
	ds_read_b128 v[82:85], v86 offset:7168
	s_waitcnt lgkmcnt(5)
	v_pk_fma_f32 v[68:69], v[26:27], v[130:131], v[16:17]
	v_pk_fma_f32 v[76:77], v[24:25], v[128:129], v[14:15]
	s_waitcnt lgkmcnt(4)
	v_pk_fma_f32 v[50:51], v[32:33], v[36:37], v[20:21]
	v_pk_fma_f32 v[60:61], v[30:31], v[34:35], v[18:19]
	s_waitcnt lgkmcnt(1)
	v_pk_fma_f32 v[34:35], v[134:135], v[66:67], v[42:43]
	v_pk_fma_f32 v[42:43], v[132:133], v[64:65], v[40:41]
	s_waitcnt lgkmcnt(0)
	v_pk_fma_f32 v[18:19], v[138:139], v[84:85], v[48:49]
	v_pk_fma_f32 v[26:27], v[136:137], v[82:83], v[46:47]
	v_bfe_u32 v14, v76, 16, 1
	v_bfe_u32 v16, v68, 16, 1
	v_bfe_u32 v15, v77, 16, 1
	v_bfe_u32 v17, v69, 16, 1
	v_bfe_u32 v20, v60, 16, 1
	v_bfe_u32 v24, v50, 16, 1
	v_bfe_u32 v30, v42, 16, 1
	v_bfe_u32 v32, v34, 16, 1
	v_bfe_u32 v36, v26, 16, 1
	v_bfe_u32 v40, v18, 16, 1
	v_add3_u32 v14, v76, v14, s22
	v_add3_u32 v16, v68, v16, s22
	v_bfe_u32 v21, v61, 16, 1
	v_bfe_u32 v25, v51, 16, 1
	v_bfe_u32 v31, v43, 16, 1
	v_bfe_u32 v33, v35, 16, 1
	v_bfe_u32 v37, v27, 16, 1
	v_bfe_u32 v41, v19, 16, 1
	v_max_f32_e64 v46, |v76|, |v77|
	v_max_f32_e64 v47, |v68|, |v69|
	v_add3_u32 v15, v77, v15, s22
	v_add3_u32 v17, v69, v17, s22
	v_add3_u32 v20, v60, v20, s22
	v_add3_u32 v24, v50, v24, s22
	v_add3_u32 v30, v42, v30, s22
	v_add3_u32 v32, v34, v32, s22
	v_add3_u32 v36, v26, v36, s22
	v_add3_u32 v40, v18, v40, s22
	v_lshrrev_b32_e32 v14, 16, v14
	v_lshrrev_b32_e32 v16, 16, v16
	v_max_f32_e64 v48, |v60|, |v61|
	v_max_f32_e64 v49, |v50|, |v51|
	v_add3_u32 v21, v61, v21, s22
	v_add3_u32 v25, v51, v25, s22
	v_add3_u32 v31, v43, v31, s22
	v_add3_u32 v33, v35, v33, s22
	v_add3_u32 v37, v27, v37, s22
	v_add3_u32 v41, v19, v41, s22
	v_max3_f32 v46, v58, v46, v47
	v_lshrrev_b32_e32 v20, 16, v20
	v_lshrrev_b32_e32 v24, 16, v24
	v_lshrrev_b32_e32 v30, 16, v30
	v_lshrrev_b32_e32 v32, 16, v32
	v_lshrrev_b32_e32 v36, 16, v36
	v_lshrrev_b32_e32 v40, 16, v40
	v_and_or_b32 v14, v15, s21, v14
	v_and_or_b32 v15, v17, s21, v16
	v_max_f32_e64 v59, |v42|, |v43|
	v_max_f32_e64 v64, |v34|, |v35|
	v_max3_f32 v46, v46, v48, v49
	v_and_or_b32 v16, v21, s21, v20
	v_and_or_b32 v17, v25, s21, v24
	v_and_or_b32 v20, v31, s21, v30
	v_and_or_b32 v21, v33, s21, v32
	v_and_or_b32 v24, v37, s21, v36
	v_and_or_b32 v25, v41, s21, v40
	global_store_dwordx2 v[74:75], v[14:15], off offset:2048
	global_store_dwordx2 v[74:75], v[16:17], off offset:2560
	global_store_dwordx2 v[74:75], v[20:21], off offset:3072
	global_store_dwordx2 v[74:75], v[24:25], off offset:3584
	v_max_f32_e64 v65, |v26|, |v27|
	v_max_f32_e64 v66, |v18|, |v19|
	v_max3_f32 v30, v46, v59, v64
	v_max3_f32 v20, v30, v65, v66
	ds_read_b128 v[14:17], v86 offset:24576
	ds_read_b128 v[30:33], v86 offset:25600
	ds_read_b128 v[46:49], v86 offset:8192
	ds_read_b128 v[82:85], v86 offset:9216
	ds_read_b128 v[96:99], v86 offset:26624
	ds_read_b128 v[100:103], v86 offset:27648
	ds_read_b128 v[104:107], v86 offset:10240
	ds_read_b128 v[108:111], v86 offset:11264
	s_waitcnt lgkmcnt(5)
	v_pk_fma_f32 v[66:67], v[142:143], v[48:49], v[16:17]
	v_pk_fma_f32 v[74:75], v[140:141], v[46:47], v[14:15]
	s_waitcnt lgkmcnt(4)
	v_pk_fma_f32 v[48:49], v[144:145], v[84:85], v[32:33]
	v_pk_fma_f32 v[58:59], v[54:55], v[82:83], v[30:31]
	s_waitcnt lgkmcnt(1)
	v_pk_fma_f32 v[32:33], v[148:149], v[106:107], v[98:99]
	v_pk_fma_f32 v[40:41], v[146:147], v[104:105], v[96:97]
	s_waitcnt lgkmcnt(0)
	v_pk_fma_f32 v[16:17], v[152:153], v[110:111], v[102:103]
	v_pk_fma_f32 v[24:25], v[150:151], v[108:109], v[100:101]
	v_bfe_u32 v14, v74, 16, 1
	v_bfe_u32 v21, v66, 16, 1
	v_bfe_u32 v15, v75, 16, 1
	v_bfe_u32 v30, v67, 16, 1
	v_bfe_u32 v31, v58, 16, 1
	v_bfe_u32 v37, v48, 16, 1
	v_bfe_u32 v47, v40, 16, 1
	v_bfe_u32 v55, v32, 16, 1
	v_bfe_u32 v65, v24, 16, 1
	v_bfe_u32 v71, v16, 16, 1
	v_add3_u32 v14, v74, v14, s22
	v_add3_u32 v21, v66, v21, s22
	v_bfe_u32 v36, v59, 16, 1
	v_bfe_u32 v46, v49, 16, 1
	v_bfe_u32 v54, v41, 16, 1
	v_bfe_u32 v64, v33, 16, 1
	v_bfe_u32 v70, v25, 16, 1
	v_bfe_u32 v82, v17, 16, 1
	v_max_f32_e64 v83, |v74|, |v75|
	v_max_f32_e64 v84, |v66|, |v67|
	v_add3_u32 v15, v75, v15, s22
	v_add3_u32 v30, v67, v30, s22
	v_add3_u32 v31, v58, v31, s22
	v_add3_u32 v37, v48, v37, s22
	v_add3_u32 v47, v40, v47, s22
	v_add3_u32 v55, v32, v55, s22
	v_add3_u32 v65, v24, v65, s22
	v_add3_u32 v71, v16, v71, s22
	v_lshrrev_b32_e32 v14, 16, v14
	v_lshrrev_b32_e32 v21, 16, v21
	v_max_f32_e64 v85, |v58|, |v59|
	v_max_f32_e64 v95, |v48|, |v49|
	v_add3_u32 v36, v59, v36, s22
	v_add3_u32 v46, v49, v46, s22
	v_add3_u32 v54, v41, v54, s22
	v_add3_u32 v64, v33, v64, s22
	v_add3_u32 v70, v25, v70, s22
	v_add3_u32 v82, v17, v82, s22
	v_max3_f32 v20, v20, v83, v84
	v_lshrrev_b32_e32 v31, 16, v31
	v_lshrrev_b32_e32 v37, 16, v37
	v_lshrrev_b32_e32 v47, 16, v47
	v_lshrrev_b32_e32 v55, 16, v55
	v_lshrrev_b32_e32 v65, 16, v65
	v_lshrrev_b32_e32 v71, 16, v71
	v_and_or_b32 v14, v15, s21, v14
	v_and_or_b32 v15, v30, s21, v21
	v_max_f32_e64 v96, |v40|, |v41|
	v_max_f32_e64 v97, |v32|, |v33|
	v_max3_f32 v83, v20, v85, v95
	v_and_or_b32 v20, v36, s21, v31
	v_and_or_b32 v21, v46, s21, v37
	v_and_or_b32 v30, v54, s21, v47
	v_and_or_b32 v31, v64, s21, v55
	v_and_or_b32 v36, v70, s21, v65
	v_and_or_b32 v37, v82, s21, v71
	global_store_dwordx2 v[80:81], v[14:15], off
	global_store_dwordx2 v[80:81], v[20:21], off offset:512
	global_store_dwordx2 v[80:81], v[30:31], off offset:1024
	global_store_dwordx2 v[80:81], v[36:37], off offset:1536
	v_max_f32_e64 v98, |v24|, |v25|
	v_max_f32_e64 v99, |v16|, |v17|
	v_max3_f32 v46, v83, v96, v97
	v_max3_f32 v95, v46, v98, v99
	ds_read_b128 v[82:85], v86 offset:28672
	ds_read_b128 v[96:99], v86 offset:29696
	ds_read_b128 v[100:103], v86 offset:12288
	ds_read_b128 v[104:107], v86 offset:13312
	ds_read_b128 v[108:111], v86 offset:30720
	ds_read_b128 v[112:115], v86 offset:31744
	ds_read_b128 v[116:119], v86 offset:14336
	ds_read_b128 v[120:123], v86 offset:15360
	s_waitcnt lgkmcnt(5)
	v_pk_fma_f32 v[64:65], v[164:165], v[102:103], v[84:85]
	v_pk_fma_f32 v[70:71], v[162:163], v[100:101], v[82:83]
	s_waitcnt lgkmcnt(4)
	v_pk_fma_f32 v[46:47], v[168:169], v[106:107], v[98:99]
	v_pk_fma_f32 v[54:55], v[166:167], v[104:105], v[96:97]
	s_waitcnt lgkmcnt(1)
	v_pk_fma_f32 v[36:37], v[170:171], v[116:117], v[108:109]
	v_max_f32_e64 v108, |v70|, |v71|
	v_max_f32_e64 v109, |v64|, |v65|
	v_pk_fma_f32 v[30:31], v[172:173], v[118:119], v[110:111]
	v_max_f32_e64 v110, |v54|, |v55|
	v_max_f32_e64 v111, |v46|, |v47|
	v_max3_f32 v95, v95, v108, v109
	s_waitcnt lgkmcnt(0)
	v_pk_fma_f32 v[14:15], v[176:177], v[122:123], v[114:115]
	v_pk_fma_f32 v[20:21], v[174:175], v[120:121], v[112:113]
	v_max_f32_e64 v112, |v36|, |v37|
	v_max_f32_e64 v113, |v30|, |v31|
	v_max3_f32 v95, v95, v110, v111
	v_max_f32_e64 v114, |v20|, |v21|
	v_max_f32_e64 v115, |v14|, |v15|
	v_max3_f32 v95, v95, v112, v113
	v_max3_f32 v95, v95, v114, v115
	ds_bpermute_b32 v108, v92, v95
	v_bfe_u32 v82, v70, 16, 1
	v_bfe_u32 v84, v64, 16, 1
	v_bfe_u32 v96, v54, 16, 1
	v_bfe_u32 v83, v71, 16, 1
	s_waitcnt lgkmcnt(0)
	v_max_f32_e32 v108, v108, v108
	v_max_f32_e32 v95, v95, v108
	ds_bpermute_b32 v108, v91, v95
	v_bfe_u32 v85, v65, 16, 1
	v_bfe_u32 v97, v55, 16, 1
	v_add3_u32 v82, v70, v82, s22
	v_add3_u32 v84, v64, v84, s22
	s_waitcnt lgkmcnt(0)
	v_max_f32_e32 v108, v108, v108
	v_max_f32_e32 v95, v95, v108
	ds_bpermute_b32 v108, v90, v95
	v_add3_u32 v96, v54, v96, s22
	v_add3_u32 v83, v71, v83, s22
	v_add3_u32 v85, v65, v85, s22
	v_add3_u32 v97, v55, v97, s22
	s_waitcnt lgkmcnt(0)
	v_max_f32_e32 v108, v108, v108
	v_max_f32_e32 v95, v95, v108
	ds_bpermute_b32 v108, v89, v95
	v_lshrrev_b32_e32 v82, 16, v82
	v_lshrrev_b32_e32 v84, 16, v84
	v_lshrrev_b32_e32 v96, 16, v96
	v_and_or_b32 v82, v83, s21, v82
	v_and_or_b32 v83, v85, s21, v84
	v_and_or_b32 v84, v97, s21, v96
	s_waitcnt lgkmcnt(0)
	v_max_f32_e32 v96, v108, v108
	v_max_f32_e32 v95, v95, v96
	ds_bpermute_b32 v108, v94, v95
	v_bfe_u32 v100, v36, 16, 1
	v_bfe_u32 v101, v37, 16, 1
	v_add3_u32 v100, v36, v100, s22
	v_add3_u32 v101, v37, v101, s22
	v_lshrrev_b32_e32 v100, 16, v100
	v_and_or_b32 v96, v101, s21, v100
	s_waitcnt lgkmcnt(0)
	v_max_f32_e32 v100, v108, v108
	v_max_f32_e32 v95, v95, v100
	ds_bpermute_b32 v100, v93, v95
	v_bfe_u32 v98, v46, 16, 1
	v_bfe_u32 v102, v30, 16, 1
	v_bfe_u32 v104, v20, 16, 1
	v_bfe_u32 v106, v14, 16, 1
	v_bfe_u32 v99, v47, 16, 1
	v_bfe_u32 v103, v31, 16, 1
	v_bfe_u32 v105, v21, 16, 1
	v_bfe_u32 v107, v15, 16, 1
	v_add3_u32 v98, v46, v98, s22
	v_add3_u32 v102, v30, v102, s22
	v_add3_u32 v104, v20, v104, s22
	v_add3_u32 v106, v14, v106, s22
	v_add3_u32 v99, v47, v99, s22
	v_add3_u32 v103, v31, v103, s22
	v_add3_u32 v105, v21, v105, s22
	v_add3_u32 v107, v15, v107, s22
	v_lshrrev_b32_e32 v98, 16, v98
	v_lshrrev_b32_e32 v102, 16, v102
	v_lshrrev_b32_e32 v104, 16, v104
	v_lshrrev_b32_e32 v106, 16, v106
	v_and_or_b32 v85, v99, s21, v98
	v_and_or_b32 v97, v103, s21, v102
	v_and_or_b32 v98, v105, s21, v104
	v_and_or_b32 v99, v107, s21, v106
	global_store_dwordx2 v[80:81], v[82:83], off offset:2048
	global_store_dwordx2 v[80:81], v[84:85], off offset:2560
	global_store_dwordx2 v[80:81], v[96:97], off offset:3072
	global_store_dwordx2 v[80:81], v[98:99], off offset:3584
	s_waitcnt lgkmcnt(0)
	v_max3_f32 v80, v95, v100, s26
	v_mul_f32_e32 v80, 0x3c09ae41, v80
	v_div_scale_f32 v81, s[18:19], v80, v80, 1.0
	v_rcp_f32_e32 v82, v81
	v_div_scale_f32 v83, vcc, 1.0, v80, 1.0
	v_fma_f32 v84, -v81, v82, 1.0
	v_fmac_f32_e32 v82, v84, v82
	v_mul_f32_e32 v84, v83, v82
	v_fma_f32 v85, -v81, v84, v83
	v_fmac_f32_e32 v84, v85, v82
	v_fma_f32 v81, -v81, v84, v83
	v_div_fmas_f32 v81, v81, v82, v84
	v_div_fixup_f32 v81, v81, v80, 1.0
	v_mul_f32_e32 v78, v78, v81
	v_mul_f32_e32 v79, v79, v81
	v_mul_f32_e32 v72, v72, v81
	v_mul_f32_e32 v73, v73, v81
	v_rndne_f32_e32 v78, v78
	v_rndne_f32_e32 v79, v79
	v_mul_f32_e32 v62, v62, v81
	v_mul_f32_e32 v63, v63, v81
	v_mul_f32_e32 v57, v57, v81
	v_rndne_f32_e32 v72, v72
	v_rndne_f32_e32 v73, v73
	v_cvt_i32_f32_e32 v78, v78
	v_cvt_i32_f32_e32 v79, v79
	v_mul_f32_e32 v56, v56, v81
	v_rndne_f32_e32 v62, v62
	v_rndne_f32_e32 v63, v63
	v_rndne_f32_e32 v57, v57
	v_cvt_i32_f32_e32 v72, v72
	v_cvt_i32_f32_e32 v73, v73
	v_mul_f32_e32 v44, v44, v81
	v_mul_f32_e32 v45, v45, v81
	v_mul_f32_e32 v39, v39, v81
	v_rndne_f32_e32 v56, v56
	v_cvt_i32_f32_e32 v62, v62
	v_cvt_i32_f32_e32 v63, v63
	v_cvt_i32_f32_e32 v57, v57
	v_mul_f32_e32 v38, v38, v81
	v_rndne_f32_e32 v44, v44
	v_rndne_f32_e32 v45, v45
	v_rndne_f32_e32 v39, v39
	v_cvt_i32_f32_e32 v56, v56
	v_mul_f32_e32 v28, v28, v81
	v_mul_f32_e32 v29, v29, v81
	v_mul_f32_e32 v22, v22, v81
	v_mul_f32_e32 v23, v23, v81
	v_mul_f32_e32 v76, v76, v81
	v_mul_f32_e32 v77, v77, v81
	v_mul_f32_e32 v68, v68, v81
	v_mul_f32_e32 v69, v69, v81
	v_mul_f32_e32 v60, v60, v81
	v_mul_f32_e32 v61, v61, v81
	v_mul_f32_e32 v50, v50, v81
	v_mul_f32_e32 v51, v51, v81
	v_mul_f32_e32 v42, v42, v81
	v_mul_f32_e32 v43, v43, v81
	v_mul_f32_e32 v34, v34, v81
	v_mul_f32_e32 v35, v35, v81
	v_mul_f32_e32 v26, v26, v81
	v_mul_f32_e32 v27, v27, v81
	v_mul_f32_e32 v18, v18, v81
	v_mul_f32_e32 v19, v19, v81
	v_mul_f32_e32 v74, v74, v81
	v_mul_f32_e32 v75, v75, v81
	v_mul_f32_e32 v66, v66, v81
	v_mul_f32_e32 v67, v67, v81
	v_mul_f32_e32 v58, v58, v81
	v_mul_f32_e32 v59, v59, v81
	v_mul_f32_e32 v48, v48, v81
	v_mul_f32_e32 v49, v49, v81
	v_mul_f32_e32 v40, v40, v81
	v_mul_f32_e32 v41, v41, v81
	v_mul_f32_e32 v32, v32, v81
	v_mul_f32_e32 v33, v33, v81
	v_mul_f32_e32 v24, v24, v81
	v_mul_f32_e32 v25, v25, v81
	v_mul_f32_e32 v16, v16, v81
	v_mul_f32_e32 v17, v17, v81
	v_mul_f32_e32 v70, v70, v81
	v_mul_f32_e32 v71, v71, v81
	v_mul_f32_e32 v64, v64, v81
	v_mul_f32_e32 v65, v65, v81
	v_mul_f32_e32 v54, v54, v81
	v_mul_f32_e32 v55, v55, v81
	v_mul_f32_e32 v46, v46, v81
	v_mul_f32_e32 v47, v47, v81
	v_mul_f32_e32 v36, v36, v81
	v_mul_f32_e32 v37, v37, v81
	v_mul_f32_e32 v30, v30, v81
	v_mul_f32_e32 v31, v31, v81
	v_mul_f32_e32 v20, v20, v81
	v_mul_f32_e32 v21, v21, v81
	v_mul_f32_e32 v14, v14, v81
	v_mul_f32_e32 v15, v15, v81
	v_rndne_f32_e32 v38, v38
	v_cvt_i32_f32_e32 v44, v44
	v_cvt_i32_f32_e32 v45, v45
	v_cvt_i32_f32_e32 v39, v39
	v_add_u32_e32 v81, v79, v78
	v_rndne_f32_e32 v28, v28
	v_rndne_f32_e32 v29, v29
	v_rndne_f32_e32 v23, v23
	v_cvt_i32_f32_e32 v38, v38
	v_lshlrev_b32_e32 v82, 16, v72
	v_add3_u32 v72, v81, v73, v72
	v_rndne_f32_e32 v22, v22
	v_cvt_i32_f32_e32 v28, v28
	v_cvt_i32_f32_e32 v29, v29
	v_cvt_i32_f32_e32 v23, v23
	v_perm_b32 v85, v57, v62, s27
	v_add3_u32 v62, v72, v63, v62
	v_rndne_f32_e32 v76, v76
	v_rndne_f32_e32 v77, v77
	v_cvt_i32_f32_e32 v22, v22
	v_lshlrev_b32_e32 v84, 16, v56
	v_add3_u32 v56, v62, v57, v56
	v_rndne_f32_e32 v68, v68
	v_rndne_f32_e32 v69, v69
	v_cvt_i32_f32_e32 v76, v76
	v_cvt_i32_f32_e32 v77, v77
	v_perm_b32 v97, v39, v44, s27
	v_add3_u32 v44, v56, v45, v44
	v_rndne_f32_e32 v60, v60
	v_rndne_f32_e32 v61, v61
	v_cvt_i32_f32_e32 v68, v68
	v_cvt_i32_f32_e32 v69, v69
	v_lshlrev_b32_e32 v96, 16, v38
	v_add3_u32 v38, v44, v39, v38
	v_rndne_f32_e32 v50, v50
	v_rndne_f32_e32 v51, v51
	v_cvt_i32_f32_e32 v60, v60
	v_cvt_i32_f32_e32 v61, v61
	v_perm_b32 v100, v23, v28, s27
	v_add3_u32 v28, v38, v29, v28
	v_rndne_f32_e32 v42, v42
	v_rndne_f32_e32 v43, v43
	v_cvt_i32_f32_e32 v50, v50
	v_cvt_i32_f32_e32 v51, v51
	v_lshlrev_b32_e32 v99, 16, v22
	v_add3_u32 v22, v28, v23, v22
	v_rndne_f32_e32 v34, v34
	v_rndne_f32_e32 v35, v35
	v_cvt_i32_f32_e32 v42, v42
	v_cvt_i32_f32_e32 v43, v43
	v_add3_u32 v22, v22, v77, v76
	v_rndne_f32_e32 v26, v26
	v_rndne_f32_e32 v27, v27
	v_cvt_i32_f32_e32 v34, v34
	v_cvt_i32_f32_e32 v35, v35
	v_add3_u32 v22, v22, v69, v68
	v_rndne_f32_e32 v18, v18
	v_rndne_f32_e32 v19, v19
	v_cvt_i32_f32_e32 v26, v26
	v_cvt_i32_f32_e32 v27, v27
	v_add3_u32 v22, v22, v61, v60
	v_rndne_f32_e32 v74, v74
	v_rndne_f32_e32 v75, v75
	v_cvt_i32_f32_e32 v18, v18
	v_cvt_i32_f32_e32 v19, v19
	v_add3_u32 v22, v22, v51, v50
	v_rndne_f32_e32 v66, v66
	v_rndne_f32_e32 v67, v67
	v_cvt_i32_f32_e32 v74, v74
	v_cvt_i32_f32_e32 v75, v75
	v_add3_u32 v22, v22, v43, v42
	v_rndne_f32_e32 v58, v58
	v_rndne_f32_e32 v59, v59
	v_cvt_i32_f32_e32 v66, v66
	v_cvt_i32_f32_e32 v67, v67
	v_add3_u32 v22, v22, v35, v34
	v_rndne_f32_e32 v48, v48
	v_rndne_f32_e32 v49, v49
	v_cvt_i32_f32_e32 v58, v58
	v_cvt_i32_f32_e32 v59, v59
	v_add3_u32 v22, v22, v27, v26
	v_rndne_f32_e32 v40, v40
	v_rndne_f32_e32 v41, v41
	v_cvt_i32_f32_e32 v48, v48
	v_cvt_i32_f32_e32 v49, v49
	v_lshlrev_b32_e32 v111, 16, v18
	v_add3_u32 v18, v22, v19, v18
	v_rndne_f32_e32 v32, v32
	v_rndne_f32_e32 v33, v33
	v_cvt_i32_f32_e32 v40, v40
	v_cvt_i32_f32_e32 v41, v41
	v_add3_u32 v18, v18, v75, v74
	v_rndne_f32_e32 v24, v24
	v_rndne_f32_e32 v25, v25
	v_cvt_i32_f32_e32 v32, v32
	v_cvt_i32_f32_e32 v33, v33
	v_add3_u32 v18, v18, v67, v66
	v_rndne_f32_e32 v16, v16
	v_rndne_f32_e32 v17, v17
	v_cvt_i32_f32_e32 v24, v24
	v_cvt_i32_f32_e32 v25, v25
	v_add3_u32 v18, v18, v59, v58
	v_rndne_f32_e32 v70, v70
	v_rndne_f32_e32 v71, v71
	v_cvt_i32_f32_e32 v16, v16
	v_cvt_i32_f32_e32 v17, v17
	v_add3_u32 v18, v18, v49, v48
	v_rndne_f32_e32 v64, v64
	v_rndne_f32_e32 v65, v65
	v_cvt_i32_f32_e32 v70, v70
	v_cvt_i32_f32_e32 v71, v71
	v_add3_u32 v18, v18, v41, v40
	v_rndne_f32_e32 v54, v54
	v_rndne_f32_e32 v55, v55
	v_cvt_i32_f32_e32 v64, v64
	v_cvt_i32_f32_e32 v65, v65
	v_add3_u32 v18, v18, v33, v32
	v_rndne_f32_e32 v46, v46
	v_rndne_f32_e32 v47, v47
	v_cvt_i32_f32_e32 v54, v54
	v_cvt_i32_f32_e32 v55, v55
	v_add3_u32 v18, v18, v25, v24
	v_rndne_f32_e32 v36, v36
	v_rndne_f32_e32 v37, v37
	v_cvt_i32_f32_e32 v46, v46
	v_cvt_i32_f32_e32 v47, v47
	v_lshlrev_b32_e32 v123, 16, v16
	v_add3_u32 v16, v18, v17, v16
	v_rndne_f32_e32 v30, v30
	v_rndne_f32_e32 v31, v31
	v_cvt_i32_f32_e32 v36, v36
	v_cvt_i32_f32_e32 v37, v37
	v_add3_u32 v16, v16, v71, v70
	v_rndne_f32_e32 v20, v20
	v_rndne_f32_e32 v21, v21
	v_cvt_i32_f32_e32 v30, v30
	v_cvt_i32_f32_e32 v31, v31
	v_add3_u32 v16, v16, v65, v64
	v_rndne_f32_e32 v14, v14
	v_rndne_f32_e32 v15, v15
	v_cvt_i32_f32_e32 v20, v20
	v_cvt_i32_f32_e32 v21, v21
	v_add3_u32 v16, v16, v55, v54
	v_cvt_i32_f32_e32 v14, v14
	v_perm_b32 v124, v17, v24, s27
	v_add3_u32 v16, v16, v47, v46
	v_cvt_i32_f32_e32 v17, v15
	v_add3_u32 v15, v16, v37, v36
	v_add3_u32 v15, v15, v31, v30
	v_add3_u32 v15, v15, v21, v20
	v_add3_u32 v15, v15, v17, v14
	ds_bpermute_b32 v16, v92, v15
	v_lshlrev_b32_e32 v79, 8, v79
	v_lshlrev_b32_e32 v83, 8, v63
	v_lshlrev_b32_e32 v95, 8, v45
	v_lshlrev_b32_e32 v98, 8, v29
	s_waitcnt lgkmcnt(0)
	v_add_u32_e32 v15, v15, v16
	ds_bpermute_b32 v16, v91, v15
	v_lshlrev_b32_e32 v101, 8, v77
	v_lshlrev_b32_e32 v102, 16, v68
	v_lshlrev_b32_e32 v104, 8, v61
	v_lshlrev_b32_e32 v105, 16, v50
	s_waitcnt lgkmcnt(0)
	v_add_u32_e32 v15, v15, v16
	ds_bpermute_b32 v16, v90, v15
	v_lshlrev_b32_e32 v107, 8, v43
	v_lshlrev_b32_e32 v108, 16, v34
	v_lshlrev_b32_e32 v110, 8, v27
	v_lshlrev_b32_e32 v113, 8, v75
	s_waitcnt lgkmcnt(0)
	v_add_u32_e32 v15, v15, v16
	ds_bpermute_b32 v16, v89, v15
	v_lshlrev_b32_e32 v114, 16, v66
	v_lshlrev_b32_e32 v116, 8, v59
	v_lshlrev_b32_e32 v117, 16, v48
	v_lshlrev_b32_e32 v119, 8, v41
	v_lshlrev_b32_e32 v120, 16, v32
	v_lshlrev_b32_e32 v122, 8, v25
	v_lshlrev_b32_e32 v125, 8, v71
	v_lshlrev_b32_e32 v126, 16, v64
	v_perm_b32 v78, v73, v78, s27
	v_and_b32_e32 v73, 0xff00, v79
	v_and_b32_e32 v79, 0xff0000, v82
	v_and_b32_e32 v81, 0xff00, v83
	v_and_b32_e32 v82, 0xff0000, v84
	v_and_b32_e32 v83, 0xff00, v95
	v_and_b32_e32 v84, 0xff0000, v96
	v_and_b32_e32 v95, 0xff00, v98
	v_and_b32_e32 v96, 0xff0000, v99
	v_and_b32_e32 v98, 0xff00, v101
	v_and_b32_e32 v99, 0xff0000, v102
	v_and_b32_e32 v101, 0xff00, v104
	v_and_b32_e32 v102, 0xff0000, v105
	v_and_b32_e32 v104, 0xff00, v107
	v_and_b32_e32 v105, 0xff0000, v108
	v_and_b32_e32 v107, 0xff00, v110
	v_and_b32_e32 v108, 0xff0000, v111
	v_and_b32_e32 v110, 0xff00, v113
	v_and_b32_e32 v111, 0xff0000, v114
	v_and_b32_e32 v113, 0xff00, v116
	v_and_b32_e32 v114, 0xff0000, v117
	v_and_b32_e32 v116, 0xff00, v119
	v_and_b32_e32 v117, 0xff0000, v120
	v_and_b32_e32 v119, 0xff00, v122
	v_and_b32_e32 v120, 0xff0000, v123
	v_and_b32_e32 v122, 0xff00, v125
	v_and_b32_e32 v123, 0xff0000, v126
	v_perm_b32 v18, v65, v70, s27
	v_perm_b32 v103, v69, v76, s27
	v_perm_b32 v106, v51, v60, s27
	v_perm_b32 v109, v35, v42, s27
	v_perm_b32 v112, v19, v26, s27
	v_perm_b32 v115, v67, v74, s27
	v_perm_b32 v118, v49, v58, s27
	v_perm_b32 v121, v33, v40, s27
	v_or3_b32 v73, v78, v73, v79
	v_or3_b32 v63, v85, v81, v82
	v_or3_b32 v18, v18, v122, v123
	s_waitcnt lgkmcnt(0)
	v_add_u32_e32 v15, v15, v16
	v_or3_b32 v72, v97, v83, v84
	v_or3_b32 v78, v100, v95, v96
	v_or3_b32 v79, v103, v98, v99
	v_or3_b32 v81, v106, v101, v102
	v_or3_b32 v82, v109, v104, v105
	v_or3_b32 v83, v112, v107, v108
	v_or3_b32 v84, v115, v110, v111
	v_or3_b32 v85, v118, v113, v114
	v_or3_b32 v95, v121, v116, v117
	v_or3_b32 v96, v124, v119, v120
	global_store_dword v[52:53], v73, off
	global_store_dword v[52:53], v63, off offset:256
	global_store_dword v[52:53], v72, off offset:512
	global_store_dword v[52:53], v78, off offset:768
	global_store_dword v[52:53], v79, off offset:1024
	global_store_dword v[52:53], v81, off offset:1280
	global_store_dword v[52:53], v82, off offset:1536
	global_store_dword v[52:53], v83, off offset:1792
	global_store_dword v[52:53], v84, off offset:2048
	global_store_dword v[52:53], v85, off offset:2304
	global_store_dword v[52:53], v95, off offset:2560
	global_store_dword v[52:53], v96, off offset:2816
	global_store_dword v[52:53], v18, off offset:3072
	v_lshlrev_b32_e32 v18, 8, v55
	v_lshlrev_b32_e32 v19, 16, v46
	ds_bpermute_b32 v16, v94, v15
	v_and_b32_e32 v18, 0xff00, v18
	v_and_b32_e32 v19, 0xff0000, v19
	v_perm_b32 v22, v47, v54, s27
	v_or3_b32 v18, v22, v18, v19
	global_store_dword v[52:53], v18, off offset:3328
	v_lshlrev_b32_e32 v18, 8, v37
	v_lshlrev_b32_e32 v19, 16, v30
	v_and_b32_e32 v18, 0xff00, v18
	v_and_b32_e32 v19, 0xff0000, v19
	v_perm_b32 v22, v31, v36, s27
	v_or3_b32 v18, v22, v18, v19
	v_lshlrev_b32_e32 v19, 16, v14
	s_waitcnt lgkmcnt(0)
	v_add_u32_e32 v14, v15, v16
	ds_bpermute_b32 v15, v93, v14
	global_store_dword v[52:53], v18, off offset:3584
	v_lshlrev_b32_e32 v18, 8, v21
	v_and_b32_e32 v18, 0xff00, v18
	v_and_b32_e32 v16, 0xff0000, v19
	v_perm_b32 v17, v17, v20, s27
	v_or3_b32 v16, v17, v18, v16
	global_store_dword v[52:53], v16, off offset:3840
	s_and_saveexec_b64 s[18:19], s[8:9]
	s_cbranch_execz .LBB0_1672
	v_lshlrev_b64 v[16:17], 2, v[2:3]
	v_lshl_add_u64 v[18:19], s[12:13], 0, v[16:17]
	v_lshl_add_u64 v[16:17], s[14:15], 0, v[16:17]
	s_waitcnt lgkmcnt(0)
	v_add_u32_e32 v3, v14, v15
	global_store_dword v[18:19], v80, off
	global_store_dword v[16:17], v3, off
	s_branch .LBB0_1672
